# MLA step: tile DMAs issued after the 12 K-fragment LDS reads instead of in front of them
# baseline (speedup 1.0000x reference)
.LBB0_1455:
.LBB0_1456:
	s_add_i32 s2, s79, 1
	s_and_b32 s2, s2, 3
	s_mulk_i32 s2, 0x3000
	v_add_u32_e32 v72, s2, v168
	ds_read_b128 v[68:71], v72
	ds_read_b128 v[172:175], v72 offset:512
	ds_read_b128 v[176:179], v72 offset:2048
	ds_read_b128 v[180:183], v72 offset:2560
	ds_read_b128 v[184:187], v72 offset:4096
	ds_read_b128 v[190:193], v72 offset:4608
	ds_read_b128 v[212:215], v72 offset:6144
	ds_read_b128 v[216:219], v72 offset:6656
	ds_read_b128 v[224:227], v72 offset:8192
	ds_read_b128 v[228:231], v72 offset:8704
	ds_read_b128 v[232:235], v72 offset:10240
	ds_read_b128 v[236:239], v72 offset:10752
	s_cmp_gt_u32 s79, 64
	s_cbranch_scc1 .Lmla_dma_skip1
	s_add_i32 s2, s79, -1
	s_and_b32 s6, s2, 3
	s_mul_i32 s7, s6, 0x3000
	v_lshl_add_u64 v[240:241], v[162:163], 0, s[88:89]
	s_add_i32 s2, s7, s9
	s_mov_b32 s3, m0
	s_mov_b32 m0, s2
	s_nop 0
	global_load_lds_dwordx4 v[240:241], off
	s_mov_b32 m0, s3
	s_movk_i32 s2, 0xf000
	s_mov_b32 s3, -1
	v_lshl_add_u64 v[240:241], v[158:159], 0, s[2:3]
	s_add_i32 s2, s7, s27
	s_mov_b32 s3, m0
	s_mov_b32 m0, s2
	s_nop 0
	global_load_lds_dwordx4 v[240:241], off
	s_mov_b32 m0, s3
	s_lshl_b32 s2, s6, 13
	v_lshl_add_u64 v[240:241], v[160:161], 0, s[88:89]
	s_add_i32 s2, s2, s26
	s_mov_b32 s3, m0
	s_mov_b32 m0, s2
	s_nop 0
	global_load_lds_dwordx4 v[240:241], off
	s_mov_b32 m0, s3
.Lmla_dma_skip1:
	s_waitcnt lgkmcnt(11)
	v_mfma_f32_32x32x16_bf16 v[100:115], v[68:71], v[116:119], v[36:51]
	v_exp_f32_e32 v84, v84
	v_exp_f32_e32 v85, v85
	v_exp_f32_e32 v86, v86
	v_exp_f32_e32 v87, v87
	s_waitcnt lgkmcnt(10)
	v_mfma_f32_32x32x16_bf16 v[68:83], v[172:175], v[116:119], v[36:51]
	v_add_f32_e64 v172, v84, 0
	v_add_f32_e64 v173, v85, 0
	v_add_f32_e64 v172, v86, v172
	v_add_f32_e64 v173, v87, v173
	s_waitcnt lgkmcnt(9)
	v_mfma_f32_32x32x16_bf16 v[100:115], v[176:179], v[120:123], v[100:115]
	v_exp_f32_e32 v88, v88
	v_exp_f32_e32 v89, v89
	v_exp_f32_e32 v90, v90
	v_exp_f32_e32 v91, v91
	v_pk_add_f32 v[172:173], v[88:89], v[172:173]
	s_nop 0
	v_pk_add_f32 v[172:173], v[90:91], v[172:173]
	s_waitcnt lgkmcnt(8)
	v_mfma_f32_32x32x16_bf16 v[68:83], v[180:183], v[120:123], v[68:83]
	s_waitcnt lgkmcnt(7)
	v_mfma_f32_32x32x16_bf16 v[100:115], v[184:187], v[124:127], v[100:115]
	v_exp_f32_e32 v92, v92
	v_exp_f32_e32 v93, v93
	v_exp_f32_e32 v94, v94
	v_exp_f32_e32 v95, v95
	v_pk_add_f32 v[172:173], v[92:93], v[172:173]
	s_nop 0
	v_pk_add_f32 v[172:173], v[94:95], v[172:173]
	s_waitcnt lgkmcnt(6)
	v_mfma_f32_32x32x16_bf16 v[68:83], v[190:193], v[124:127], v[68:83]
	s_waitcnt lgkmcnt(5)
	v_mfma_f32_32x32x16_bf16 v[100:115], v[212:215], v[128:131], v[100:115]
	v_exp_f32_e32 v96, v96
	v_exp_f32_e32 v97, v97
	v_exp_f32_e32 v98, v98
	v_exp_f32_e32 v99, v99
	v_pk_add_f32 v[172:173], v[96:97], v[172:173]
	s_nop 0
	v_pk_add_f32 v[172:173], v[98:99], v[172:173]
	s_waitcnt lgkmcnt(4)
	v_mfma_f32_32x32x16_bf16 v[68:83], v[216:219], v[128:131], v[68:83]
	v_exp_f32_e32 v174, v52
	v_exp_f32_e32 v175, v53
	s_waitcnt lgkmcnt(3)
	v_mfma_f32_32x32x16_bf16 v[100:115], v[224:227], v[132:135], v[100:115]
	v_add_f32_e64 v52, v174, v172
	v_add_f32_e64 v53, v175, v173
	v_exp_f32_e32 v172, v54
	v_exp_f32_e32 v173, v55
	s_nop 0
	v_pk_add_f32 v[52:53], v[172:173], v[52:53]
	s_waitcnt lgkmcnt(2)
	v_mfma_f32_32x32x16_bf16 v[68:83], v[228:231], v[132:135], v[68:83]
	s_waitcnt lgkmcnt(1)
	v_mfma_f32_32x32x16_bf16 v[100:115], v[232:235], v[136:139], v[100:115]
	v_exp_f32_e32 v176, v56
	v_exp_f32_e32 v177, v57
	v_exp_f32_e32 v178, v58
	v_exp_f32_e32 v179, v59
	v_pk_add_f32 v[52:53], v[176:177], v[52:53]
	s_nop 0
	v_pk_add_f32 v[194:195], v[178:179], v[52:53]
	s_waitcnt lgkmcnt(0)
	v_mfma_f32_32x32x16_bf16 v[68:83], v[236:239], v[136:139], v[68:83]
	s_and_b32 s2, s78, 0x4000
	v_add_u32_e32 v212, s2, v2
	v_cvt_pk_bf16_f32 v54, v88, v89
	ds_read_b64_tr_b16 v[88:89],v212 offset:0
	v_cvt_pk_bf16_f32 v55, v90, v91
	ds_read_b64_tr_b16 v[90:91],v212 offset:512
	v_cvt_pk_bf16_f32 v53, v86, v87
	v_cvt_pk_bf16_f32 v86, v176, v177
	ds_read_b64_tr_b16 v[176:177],v212 offset:4096
	v_cvt_pk_bf16_f32 v87, v178, v179
	ds_read_b64_tr_b16 v[178:179],v212 offset:4608
	v_cvt_pk_bf16_f32 v56, v92, v93
	ds_read_b64_tr_b16 v[92:93],v212 offset:1024
	v_cvt_pk_bf16_f32 v57, v94, v95
	ds_read_b64_tr_b16 v[94:95],v212 offset:1536
	ds_read_b64_tr_b16 v[180:181],v212 offset:5120
	ds_read_b64_tr_b16 v[182:183],v212 offset:5632
	v_cvt_pk_bf16_f32 v58, v96, v97
	ds_read_b64_tr_b16 v[96:97],v212 offset:2048
	v_cvt_pk_bf16_f32 v59, v98, v99
	ds_read_b64_tr_b16 v[98:99],v212 offset:2560
	ds_read_b64_tr_b16 v[184:185],v212 offset:6144
	ds_read_b64_tr_b16 v[186:187],v212 offset:6656
	v_cvt_pk_bf16_f32 v52, v84, v85
	v_cvt_pk_bf16_f32 v85, v172, v173
	ds_read_b64_tr_b16 v[172:173],v212 offset:3072
	v_cvt_pk_bf16_f32 v84, v174, v175
	ds_read_b64_tr_b16 v[174:175],v212 offset:3584
	ds_read_b64_tr_b16 v[190:191],v212 offset:7168
	ds_read_b64_tr_b16 v[192:193],v212 offset:7680
	s_waitcnt lgkmcnt(14)
	v_mfma_f32_32x32x16_bf16 v[4:19], v[52:55], v[88:91], v[4:19]
	s_waitcnt lgkmcnt(12)
	v_mfma_f32_32x32x16_bf16 v[20:35], v[52:55], v[176:179], v[20:35]
	v_exp_f32_e32 v52, v60
	v_exp_f32_e32 v53, v61
	v_exp_f32_e32 v60, v62
	v_exp_f32_e32 v61, v63
	v_pk_add_f32 v[54:55], v[52:53], v[194:195]
	s_nop 0
	v_pk_add_f32 v[54:55], v[60:61], v[54:55]
	s_waitcnt lgkmcnt(10)
	v_mfma_f32_32x32x16_bf16 v[4:19], v[56:59], v[92:95], v[4:19]
	v_cvt_pk_bf16_f32 v52, v52, v53
	v_cvt_pk_bf16_f32 v53, v60, v61
	s_waitcnt lgkmcnt(8)
	v_mfma_f32_32x32x16_bf16 v[20:35], v[56:59], v[180:183], v[20:35]
	v_exp_f32_e32 v56, v64
	v_exp_f32_e32 v57, v65
	v_exp_f32_e32 v58, v66
	v_exp_f32_e32 v59, v67
	v_pk_add_f32 v[54:55], v[56:57], v[54:55]
	s_nop 0
	v_pk_add_f32 v[62:63], v[58:59], v[54:55]
	v_cvt_pk_bf16_f32 v54, v56, v57
	v_add_f32_e32 v56, v62, v63
	v_add_f32_e32 v171, v171, v56
	v_cvt_pk_bf16_f32 v55, v58, v59
	s_waitcnt lgkmcnt(6)
	v_mfma_f32_32x32x16_bf16 v[4:19], v[84:87], v[96:99], v[4:19]
	v_max3_f32 v56, v100, v68, v101
	s_nop 0
	v_max3_f32 v56, v56, v69, v102
	s_nop 0
	v_max3_f32 v56, v56, v70, v103
	s_nop 0
	v_max3_f32 v56, v56, v71, v104
	s_waitcnt lgkmcnt(4)
	v_mfma_f32_32x32x16_bf16 v[20:35], v[84:87], v[184:187], v[20:35]
	v_max3_f32 v56, v56, v72, v105
	s_nop 0
	v_max3_f32 v56, v56, v73, v106
	s_nop 0
	v_max3_f32 v56, v56, v74, v107
	s_nop 0
	v_max3_f32 v56, v56, v75, v107
	s_waitcnt lgkmcnt(2)
	v_mfma_f32_32x32x16_bf16 v[4:19], v[52:55], v[172:175], v[4:19]
	s_waitcnt lgkmcnt(0)
	v_mfma_f32_32x32x16_bf16 v[20:35], v[52:55], v[190:193], v[20:35]
	v_max3_f32 v52, v56, v108, v76
	s_nop 0
	v_max3_f32 v52, v52, v109, v77
	s_nop 0
	v_max3_f32 v52, v52, v110, v78
	s_nop 0
	v_max3_f32 v52, v52, v111, v79
	s_nop 0
	v_max3_f32 v52, v52, v112, v80
	s_nop 0
	v_max3_f32 v52, v52, v113, v81
	s_nop 0
	v_max3_f32 v52, v52, v114, v82
	s_nop 0
	v_max3_f32 v52, v52, v115, v83
	s_nop 0
	v_mov_b32_e32 v53, v52
	s_nop 1
	v_permlane32_swap_b32_e32 v52, v53
	v_max_f32_e32 v53, v53, v53
	v_max_f32_e32 v52, v52, v52
	v_max_f32_e32 v52, v52, v53
	v_cmp_lt_f32_e32 vcc, s13, v52
	s_cbranch_vccz .LBB0_1460
	v_max_f32_e32 v52, v52, v52
	v_max_f32_e32 v52, 0, v52
	v_exp_f32_e64 v53, -v52
	s_and_saveexec_b64 s[6:7], s[36:37]
	ds_write_b32 v170, v53
	s_or_b64 exec, exec, s[6:7]
	v_mul_f32_e32 v171, v171, v53
	s_waitcnt lgkmcnt(0)
	v_add_u32_e32 v53, s28, v169
	ds_read_b128 v[54:57], v53
	ds_read_b128 v[58:61], v53 offset:32
	ds_read_b128 v[62:65], v53 offset:64
	ds_read_b128 v[84:87], v53 offset:96
	s_waitcnt lgkmcnt(0)
	s_waitcnt lgkmcnt(3)
	v_pk_mul_f32 v[6:7], v[6:7], v[56:57]
	s_waitcnt lgkmcnt(2)
	v_pk_mul_f32 v[8:9], v[8:9], v[58:59]
	s_waitcnt lgkmcnt(1)
	v_pk_mul_f32 v[12:13], v[12:13], v[62:63]
	s_waitcnt lgkmcnt(0)
	v_pk_mul_f32 v[16:17], v[16:17], v[84:85]
	v_pk_mul_f32 v[18:19], v[18:19], v[86:87]
	v_pk_mul_f32 v[14:15], v[14:15], v[64:65]
	v_pk_mul_f32 v[10:11], v[10:11], v[60:61]
	v_pk_mul_f32 v[4:5], v[4:5], v[54:55]
	v_pk_mul_f32 v[32:33], v[32:33], v[84:85]
	v_pk_mul_f32 v[28:29], v[28:29], v[62:63]
	v_pk_mul_f32 v[24:25], v[24:25], v[58:59]
	v_pk_mul_f32 v[34:35], v[34:35], v[86:87]
	v_pk_mul_f32 v[30:31], v[30:31], v[64:65]
	v_pk_mul_f32 v[26:27], v[26:27], v[60:61]
	v_pk_mul_f32 v[22:23], v[22:23], v[56:57]
	v_pk_mul_f32 v[20:21], v[20:21], v[54:55]
	v_sub_f32_e32 v115, v115, v52
	v_sub_f32_e32 v114, v114, v52
	v_sub_f32_e32 v113, v113, v52
	v_sub_f32_e32 v112, v112, v52
	v_sub_f32_e32 v111, v111, v52
	v_sub_f32_e32 v110, v110, v52
	v_sub_f32_e32 v109, v109, v52
	v_sub_f32_e32 v108, v108, v52
	v_sub_f32_e32 v107, v107, v52
	v_sub_f32_e32 v106, v106, v52
	v_sub_f32_e32 v105, v105, v52
	v_sub_f32_e32 v104, v104, v52
	v_sub_f32_e32 v103, v103, v52
	v_sub_f32_e32 v102, v102, v52
	v_sub_f32_e32 v101, v101, v52
	v_sub_f32_e32 v100, v100, v52
	v_sub_f32_e32 v83, v83, v52
	v_sub_f32_e32 v82, v82, v52
	v_sub_f32_e32 v81, v81, v52
	v_sub_f32_e32 v80, v80, v52
	v_sub_f32_e32 v79, v79, v52
	v_sub_f32_e32 v78, v78, v52
	v_sub_f32_e32 v77, v77, v52
	v_sub_f32_e32 v76, v76, v52
	v_sub_f32_e32 v75, v75, v52
	v_sub_f32_e32 v74, v74, v52
	v_sub_f32_e32 v73, v73, v52
	v_sub_f32_e32 v72, v72, v52
	v_sub_f32_e32 v71, v71, v52
	v_sub_f32_e32 v70, v70, v52
	v_sub_f32_e32 v69, v69, v52
	v_sub_f32_e32 v68, v68, v52
	v_sub_f32_e32 v51, v51, v52
	v_sub_f32_e32 v50, v50, v52
	v_sub_f32_e32 v49, v49, v52
	v_sub_f32_e32 v48, v48, v52
	v_sub_f32_e32 v47, v47, v52
	v_sub_f32_e32 v46, v46, v52
	v_sub_f32_e32 v45, v45, v52
	v_sub_f32_e32 v44, v44, v52
	v_sub_f32_e32 v43, v43, v52
	v_sub_f32_e32 v42, v42, v52
	v_sub_f32_e32 v41, v41, v52
	v_sub_f32_e32 v40, v40, v52
	v_sub_f32_e32 v39, v39, v52
	v_sub_f32_e32 v38, v38, v52
	v_sub_f32_e32 v37, v37, v52
	v_sub_f32_e32 v36, v36, v52

.LBB0_1463:
.LBB0_1464:
	s_add_i32 s79, s79, 2
	s_and_b32 s2, s79, 2
	s_mulk_i32 s2, 0x3000
	v_add_u32_e32 v56, s2, v168
	ds_read_b128 v[52:55], v56
	ds_read_b128 v[172:175], v56 offset:512
	ds_read_b128 v[176:179], v56 offset:2048
	ds_read_b128 v[180:183], v56 offset:2560
	ds_read_b128 v[184:187], v56 offset:4096
	ds_read_b128 v[190:193], v56 offset:4608
	ds_read_b128 v[212:215], v56 offset:6144
	ds_read_b128 v[216:219], v56 offset:6656
	ds_read_b128 v[224:227], v56 offset:8192
	ds_read_b128 v[228:231], v56 offset:8704
	ds_read_b128 v[232:235], v56 offset:10240
	ds_read_b128 v[236:239], v56 offset:10752
	s_cmp_gt_u32 s79, 65
	s_cbranch_scc1 .Lmla_dma_skip2
	s_and_b32 s2, s79, 2
	s_xor_b32 s2, s2, 2
	s_mul_i32 s3, s2, 0x3000
	s_add_i32 s6, s3, s9
	s_mov_b32 s7, m0
	s_mov_b32 m0, s6
	s_nop 0
	global_load_lds_dwordx4 v[162:163], off
	s_mov_b32 m0, s7
	s_add_i32 s3, s3, s27
	s_mov_b32 s6, m0
	s_mov_b32 m0, s3
	s_nop 0
	global_load_lds_dwordx4 v[158:159], off
	s_mov_b32 m0, s6
	s_lshl_b32 s2, s2, 13
	s_add_i32 s2, s2, s26
	s_mov_b32 s3, m0
	s_mov_b32 m0, s2
	s_nop 0
	global_load_lds_dwordx4 v[160:161], off
	s_mov_b32 m0, s3
.Lmla_dma_skip2:
	s_waitcnt lgkmcnt(11)
	v_mfma_f32_32x32x16_bf16 v[84:99], v[52:55], v[116:119], v[36:51]
	v_exp_f32_e32 v100, v100
	v_exp_f32_e32 v101, v101
	v_exp_f32_e32 v102, v102
	v_exp_f32_e32 v103, v103
	s_waitcnt lgkmcnt(10)
	v_mfma_f32_32x32x16_bf16 v[52:67], v[172:175], v[116:119], v[36:51]
	v_add_f32_e64 v172, v100, 0
	v_add_f32_e64 v173, v101, 0
	v_add_f32_e64 v172, v102, v172
	v_add_f32_e64 v173, v103, v173
	s_waitcnt lgkmcnt(9)
	v_mfma_f32_32x32x16_bf16 v[84:99], v[176:179], v[120:123], v[84:99]
	v_exp_f32_e32 v104, v104
	v_exp_f32_e32 v105, v105
	v_exp_f32_e32 v106, v106
	v_exp_f32_e32 v107, v107
	v_pk_add_f32 v[172:173], v[104:105], v[172:173]
	s_nop 0
	v_pk_add_f32 v[172:173], v[106:107], v[172:173]
	s_waitcnt lgkmcnt(8)
	v_mfma_f32_32x32x16_bf16 v[52:67], v[180:183], v[120:123], v[52:67]
	s_waitcnt lgkmcnt(7)
	v_mfma_f32_32x32x16_bf16 v[84:99], v[184:187], v[124:127], v[84:99]
	v_exp_f32_e32 v108, v108
	v_exp_f32_e32 v109, v109
	v_exp_f32_e32 v110, v110
	v_exp_f32_e32 v111, v111
	v_pk_add_f32 v[172:173], v[108:109], v[172:173]
	s_nop 0
	v_pk_add_f32 v[172:173], v[110:111], v[172:173]
	s_waitcnt lgkmcnt(6)
	v_mfma_f32_32x32x16_bf16 v[52:67], v[190:193], v[124:127], v[52:67]
	s_waitcnt lgkmcnt(5)
	v_mfma_f32_32x32x16_bf16 v[84:99], v[212:215], v[128:131], v[84:99]
	v_exp_f32_e32 v112, v112
	v_exp_f32_e32 v113, v113
	v_exp_f32_e32 v114, v114
	v_exp_f32_e32 v115, v115
	v_pk_add_f32 v[172:173], v[112:113], v[172:173]
	s_nop 0
	v_pk_add_f32 v[172:173], v[114:115], v[172:173]
	s_waitcnt lgkmcnt(4)
	v_mfma_f32_32x32x16_bf16 v[52:67], v[216:219], v[128:131], v[52:67]
	v_exp_f32_e32 v174, v68
	v_exp_f32_e32 v175, v69
	s_waitcnt lgkmcnt(3)
	v_mfma_f32_32x32x16_bf16 v[84:99], v[224:227], v[132:135], v[84:99]
	v_add_f32_e64 v68, v174, v172
	v_add_f32_e64 v69, v175, v173
	v_exp_f32_e32 v172, v70
	v_exp_f32_e32 v173, v71
	s_nop 0
	v_pk_add_f32 v[68:69], v[172:173], v[68:69]
	s_waitcnt lgkmcnt(2)
	v_mfma_f32_32x32x16_bf16 v[52:67], v[228:231], v[132:135], v[52:67]
	s_waitcnt lgkmcnt(1)
	v_mfma_f32_32x32x16_bf16 v[84:99], v[232:235], v[136:139], v[84:99]
	v_exp_f32_e32 v176, v72
	v_exp_f32_e32 v177, v73
	v_exp_f32_e32 v178, v74
	v_exp_f32_e32 v179, v75
	v_pk_add_f32 v[68:69], v[176:177], v[68:69]
	s_nop 0
	v_pk_add_f32 v[194:195], v[178:179], v[68:69]
	s_waitcnt lgkmcnt(0)
	v_mfma_f32_32x32x16_bf16 v[52:67], v[236:239], v[136:139], v[52:67]
	s_add_i32 s2, s78, 0x2000
	s_and_b32 s2, s2, 0x6000
	v_add_u32_e32 v212, s2, v2
	v_cvt_pk_bf16_f32 v70, v104, v105
	ds_read_b64_tr_b16 v[104:105],v212 offset:0
	v_cvt_pk_bf16_f32 v71, v106, v107
	ds_read_b64_tr_b16 v[106:107],v212 offset:512
	v_cvt_pk_bf16_f32 v69, v102, v103
	v_cvt_pk_bf16_f32 v102, v176, v177
	ds_read_b64_tr_b16 v[176:177],v212 offset:4096
	v_cvt_pk_bf16_f32 v103, v178, v179
	ds_read_b64_tr_b16 v[178:179],v212 offset:4608
	v_cvt_pk_bf16_f32 v72, v108, v109
	ds_read_b64_tr_b16 v[108:109],v212 offset:1024
	v_cvt_pk_bf16_f32 v73, v110, v111
	ds_read_b64_tr_b16 v[110:111],v212 offset:1536
	ds_read_b64_tr_b16 v[180:181],v212 offset:5120
	ds_read_b64_tr_b16 v[182:183],v212 offset:5632
	v_cvt_pk_bf16_f32 v74, v112, v113
	ds_read_b64_tr_b16 v[112:113],v212 offset:2048
	v_cvt_pk_bf16_f32 v75, v114, v115
	ds_read_b64_tr_b16 v[114:115],v212 offset:2560
	ds_read_b64_tr_b16 v[184:185],v212 offset:6144
	ds_read_b64_tr_b16 v[186:187],v212 offset:6656
	v_cvt_pk_bf16_f32 v68, v100, v101
	v_cvt_pk_bf16_f32 v101, v172, v173
	ds_read_b64_tr_b16 v[172:173],v212 offset:3072
	v_cvt_pk_bf16_f32 v100, v174, v175
	ds_read_b64_tr_b16 v[174:175],v212 offset:3584
	ds_read_b64_tr_b16 v[190:191],v212 offset:7168
	ds_read_b64_tr_b16 v[192:193],v212 offset:7680
	s_waitcnt lgkmcnt(14)
	v_mfma_f32_32x32x16_bf16 v[4:19], v[68:71], v[104:107], v[4:19]
	s_waitcnt lgkmcnt(12)
	v_mfma_f32_32x32x16_bf16 v[20:35], v[68:71], v[176:179], v[20:35]
	v_exp_f32_e32 v68, v76
	v_exp_f32_e32 v69, v77
	v_exp_f32_e32 v76, v78
	v_exp_f32_e32 v77, v79
	v_pk_add_f32 v[70:71], v[68:69], v[194:195]
	s_nop 0
	v_pk_add_f32 v[70:71], v[76:77], v[70:71]
	s_waitcnt lgkmcnt(10)
	v_mfma_f32_32x32x16_bf16 v[4:19], v[72:75], v[108:111], v[4:19]
	v_cvt_pk_bf16_f32 v68, v68, v69
	v_cvt_pk_bf16_f32 v69, v76, v77
	s_waitcnt lgkmcnt(8)
	v_mfma_f32_32x32x16_bf16 v[20:35], v[72:75], v[180:183], v[20:35]
	v_exp_f32_e32 v72, v80
	v_exp_f32_e32 v73, v81
	v_exp_f32_e32 v74, v82
	v_exp_f32_e32 v75, v83
	v_pk_add_f32 v[70:71], v[72:73], v[70:71]
	s_nop 0
	v_pk_add_f32 v[78:79], v[74:75], v[70:71]
	v_cvt_pk_bf16_f32 v70, v72, v73
	v_add_f32_e32 v72, v78, v79
	v_add_f32_e32 v171, v171, v72
	v_cvt_pk_bf16_f32 v71, v74, v75
	s_waitcnt lgkmcnt(6)
	v_mfma_f32_32x32x16_bf16 v[4:19], v[100:103], v[112:115], v[4:19]
	v_max3_f32 v72, v84, v52, v85
	s_nop 0
	v_max3_f32 v72, v72, v53, v86
	s_nop 0
	v_max3_f32 v72, v72, v54, v87
	s_nop 0
	v_max3_f32 v72, v72, v55, v88
	s_waitcnt lgkmcnt(4)
	v_mfma_f32_32x32x16_bf16 v[20:35], v[100:103], v[184:187], v[20:35]
	v_max3_f32 v72, v72, v56, v89
	s_nop 0
	v_max3_f32 v72, v72, v57, v90
	s_nop 0
	v_max3_f32 v72, v72, v58, v91
	s_nop 0
	v_max3_f32 v72, v72, v59, v91
	s_waitcnt lgkmcnt(2)
	v_mfma_f32_32x32x16_bf16 v[4:19], v[68:71], v[172:175], v[4:19]
	s_waitcnt lgkmcnt(0)
	v_mfma_f32_32x32x16_bf16 v[20:35], v[68:71], v[190:193], v[20:35]
	v_max3_f32 v68, v72, v92, v60
	s_nop 0
	v_max3_f32 v68, v68, v93, v61
	s_nop 0
	v_max3_f32 v68, v68, v94, v62
	s_nop 0
	v_max3_f32 v68, v68, v95, v63
	s_nop 0
	v_max3_f32 v68, v68, v96, v64
	s_nop 0
	v_max3_f32 v68, v68, v97, v65
	s_nop 0
	v_max3_f32 v68, v68, v98, v66
	s_nop 0
	v_max3_f32 v68, v68, v99, v67
	s_nop 0
	v_mov_b32_e32 v69, v68
	s_nop 1
	v_permlane32_swap_b32_e32 v68, v69
	s_andn2_b64 vcc, exec, s[62:63]
	s_cbranch_vccnz .LBB0_1451
	v_max_f32_e32 v68, v68, v68
	v_max_f32_e32 v69, v69, v69
	v_max_f32_e32 v68, v68, v69
	v_cmp_lt_f32_e32 vcc, s13, v68
	s_cbranch_vccz .LBB0_1451
	v_max_f32_e32 v68, v68, v68
	v_max_f32_e32 v68, 0, v68
	v_exp_f32_e64 v69, -v68
	s_and_saveexec_b64 s[6:7], s[36:37]
	s_cbranch_execz .LBB0_1450
	ds_write_b32 v170, v69
	s_branch .LBB0_1450
